# E2: gathers of a ring half issued two steps later (less burst overlap with the transposed reads of the other half); ids via LDS
# baseline (speedup 1.0000x reference)
.Le2_noprep:
	s_lshr_b32 s99, s38, 4
	s_add_i32 m0, s99, 0x21100
	s_mov_b64 exec, 0xffff
	global_load_lds_dwordx4 v177, s[0:1]
	s_mov_b64 exec, -1
	s_lshl_b32 s99, s43, 8
	s_cmp_eq_u32 s33, 6
	s_cselect_b32 s99, s99, 0x100
	v_add_u32_e32 v177, s99, v177
	s_lshr_b32 s99, s38, 5
	s_add_i32 m0, s99, 0x23000
	s_mov_b64 exec, 0xffff
	global_load_lds_dwordx4 v176, s[22:23]
	s_mov_b64 exec, -1
	v_add_u32_e32 v176, 0x100, v176
	global_load_dword v130, v[180:181], off
	global_load_dword v131, v[180:181], off offset:256
	global_load_dword v132, v[180:181], off offset:512
	global_load_dword v133, v[180:181], off offset:768
	ds_read_b64_tr_b4 v[118:119], v151
	ds_read_b64_tr_b4 v[120:121], v159
	s_waitcnt lgkmcnt(2)
	v_cvt_scalef32_pk_f16_fp4 v122, v114, 1.0
	v_cvt_scalef32_pk_f16_fp4 v123, v114, 1.0 op_sel:[1,0,0]
	v_cvt_scalef32_pk_f16_fp4 v124, v114, 1.0 op_sel:[0,1,0]
	v_cvt_scalef32_pk_f16_fp4 v125, v114, 1.0 op_sel:[1,1,0]
	v_cvt_scalef32_pk_f16_fp4 v126, v116, 1.0
	v_cvt_scalef32_pk_f16_fp4 v127, v116, 1.0 op_sel:[1,0,0]
	v_cvt_scalef32_pk_f16_fp4 v128, v116, 1.0 op_sel:[0,1,0]
	v_cvt_scalef32_pk_f16_fp4 v129, v116, 1.0 op_sel:[1,1,0]
	v_mfma_f32_16x16x32_f16 v[2:5], v[66:69], v[122:125], 0
	v_cvt_scalef32_pk_f16_fp4 v122, v117, 1.0
	v_cvt_scalef32_pk_f16_fp4 v123, v117, 1.0 op_sel:[1,0,0]
	v_cvt_scalef32_pk_f16_fp4 v124, v117, 1.0 op_sel:[0,1,0]
	v_cvt_scalef32_pk_f16_fp4 v125, v117, 1.0 op_sel:[1,1,0]
	v_mfma_f32_16x16x32_f16 v[6:9], v[66:69], v[126:129], 0
	v_cvt_scalef32_pk_f16_fp4 v126, v115, 1.0
	v_cvt_scalef32_pk_f16_fp4 v127, v115, 1.0 op_sel:[1,0,0]
	v_cvt_scalef32_pk_f16_fp4 v128, v115, 1.0 op_sel:[0,1,0]
	v_cvt_scalef32_pk_f16_fp4 v129, v115, 1.0 op_sel:[1,1,0]
	v_mfma_f32_16x16x32_f16 v[2:5], v[74:77], v[122:125], v[2:5]
	v_mfma_f32_16x16x32_f16 v[6:9], v[74:77], v[126:129], v[6:9]
	ds_read_b64_tr_b4 v[114:115], v152
	ds_read_b64_tr_b4 v[116:117], v160
	s_waitcnt lgkmcnt(2)
	s_add_i32 m0, s38, 0x2000
	v_mad_u32_u16 v178, v102, v198, v166
	global_load_lds_dwordx4 v178, s[40:41]
	s_add_i32 m0, s38, 0x2400
	v_mad_u32_u16 v179, v102, v198, v167 op_sel:[1,0,0,0]
	global_load_lds_dwordx4 v179, s[40:41]
	s_add_i32 m0, s38, 0x2800
	v_mad_u32_u16 v178, v103, v198, v168
	global_load_lds_dwordx4 v178, s[40:41]
	s_add_i32 m0, s38, 0x2c00
	v_mad_u32_u16 v179, v103, v198, v169 op_sel:[1,0,0,0]
	global_load_lds_dwordx4 v179, s[40:41]
	s_add_i32 m0, s38, 0x3000
	v_mad_u32_u16 v178, v104, v198, v170
	global_load_lds_dwordx4 v178, s[40:41]
	s_add_i32 m0, s38, 0x3400
	v_mad_u32_u16 v179, v104, v198, v171 op_sel:[1,0,0,0]
	global_load_lds_dwordx4 v179, s[40:41]
	s_add_i32 m0, s38, 0x3800
	v_mad_u32_u16 v178, v105, v198, v172
	global_load_lds_dwordx4 v178, s[40:41]
	s_add_i32 m0, s38, 0x3c00
	v_mad_u32_u16 v179, v105, v198, v173 op_sel:[1,0,0,0]
	global_load_lds_dwordx4 v179, s[40:41]
	v_cvt_scalef32_pk_f16_fp4 v122, v118, 1.0
	v_cvt_scalef32_pk_f16_fp4 v123, v118, 1.0 op_sel:[1,0,0]
	v_cvt_scalef32_pk_f16_fp4 v124, v118, 1.0 op_sel:[0,1,0]
	v_cvt_scalef32_pk_f16_fp4 v125, v118, 1.0 op_sel:[1,1,0]
	v_cvt_scalef32_pk_f16_fp4 v126, v120, 1.0
	v_cvt_scalef32_pk_f16_fp4 v127, v120, 1.0 op_sel:[1,0,0]
	v_cvt_scalef32_pk_f16_fp4 v128, v120, 1.0 op_sel:[0,1,0]
	v_cvt_scalef32_pk_f16_fp4 v129, v120, 1.0 op_sel:[1,1,0]
	v_mfma_f32_16x16x32_f16 v[10:13], v[66:69], v[122:125], 0
	v_cvt_scalef32_pk_f16_fp4 v122, v121, 1.0
	v_cvt_scalef32_pk_f16_fp4 v123, v121, 1.0 op_sel:[1,0,0]
	v_cvt_scalef32_pk_f16_fp4 v124, v121, 1.0 op_sel:[0,1,0]
	v_cvt_scalef32_pk_f16_fp4 v125, v121, 1.0 op_sel:[1,1,0]
	v_mfma_f32_16x16x32_f16 v[14:17], v[66:69], v[126:129], 0
	v_cvt_scalef32_pk_f16_fp4 v126, v119, 1.0
	v_cvt_scalef32_pk_f16_fp4 v127, v119, 1.0 op_sel:[1,0,0]
	v_cvt_scalef32_pk_f16_fp4 v128, v119, 1.0 op_sel:[0,1,0]
	v_cvt_scalef32_pk_f16_fp4 v129, v119, 1.0 op_sel:[1,1,0]
	v_mfma_f32_16x16x32_f16 v[10:13], v[74:77], v[122:125], v[10:13]
	v_mfma_f32_16x16x32_f16 v[14:17], v[74:77], v[126:129], v[14:17]
	ds_read_b64_tr_b4 v[118:119], v153
	ds_read_b64_tr_b4 v[120:121], v161
	s_waitcnt lgkmcnt(2)
	v_cvt_scalef32_pk_f16_fp4 v122, v114, 1.0
	v_cvt_scalef32_pk_f16_fp4 v123, v114, 1.0 op_sel:[1,0,0]
	v_cvt_scalef32_pk_f16_fp4 v124, v114, 1.0 op_sel:[0,1,0]
	v_cvt_scalef32_pk_f16_fp4 v125, v114, 1.0 op_sel:[1,1,0]
	v_cvt_scalef32_pk_f16_fp4 v126, v116, 1.0
	v_cvt_scalef32_pk_f16_fp4 v127, v116, 1.0 op_sel:[1,0,0]
	v_cvt_scalef32_pk_f16_fp4 v128, v116, 1.0 op_sel:[0,1,0]
	v_cvt_scalef32_pk_f16_fp4 v129, v116, 1.0 op_sel:[1,1,0]
	v_mfma_f32_16x16x32_f16 v[18:21], v[66:69], v[122:125], 0
	v_cvt_scalef32_pk_f16_fp4 v122, v117, 1.0
	v_cvt_scalef32_pk_f16_fp4 v123, v117, 1.0 op_sel:[1,0,0]
	v_cvt_scalef32_pk_f16_fp4 v124, v117, 1.0 op_sel:[0,1,0]
	v_cvt_scalef32_pk_f16_fp4 v125, v117, 1.0 op_sel:[1,1,0]
	v_mfma_f32_16x16x32_f16 v[22:25], v[66:69], v[126:129], 0
	v_cvt_scalef32_pk_f16_fp4 v126, v115, 1.0
	v_cvt_scalef32_pk_f16_fp4 v127, v115, 1.0 op_sel:[1,0,0]
	v_cvt_scalef32_pk_f16_fp4 v128, v115, 1.0 op_sel:[0,1,0]
	v_cvt_scalef32_pk_f16_fp4 v129, v115, 1.0 op_sel:[1,1,0]
	v_mfma_f32_16x16x32_f16 v[18:21], v[74:77], v[122:125], v[18:21]
	v_mfma_f32_16x16x32_f16 v[22:25], v[74:77], v[126:129], v[22:25]
	ds_read_b64_tr_b4 v[114:115], v154
	ds_read_b64_tr_b4 v[116:117], v162
	s_waitcnt lgkmcnt(2)
	v_cvt_scalef32_pk_f16_fp4 v122, v118, 1.0
	v_cvt_scalef32_pk_f16_fp4 v123, v118, 1.0 op_sel:[1,0,0]
	v_cvt_scalef32_pk_f16_fp4 v124, v118, 1.0 op_sel:[0,1,0]
	v_cvt_scalef32_pk_f16_fp4 v125, v118, 1.0 op_sel:[1,1,0]
	v_cvt_scalef32_pk_f16_fp4 v126, v120, 1.0
	v_cvt_scalef32_pk_f16_fp4 v127, v120, 1.0 op_sel:[1,0,0]
	v_cvt_scalef32_pk_f16_fp4 v128, v120, 1.0 op_sel:[0,1,0]
	v_cvt_scalef32_pk_f16_fp4 v129, v120, 1.0 op_sel:[1,1,0]
	v_mfma_f32_16x16x32_f16 v[26:29], v[66:69], v[122:125], 0
	v_cvt_scalef32_pk_f16_fp4 v122, v121, 1.0
	v_cvt_scalef32_pk_f16_fp4 v123, v121, 1.0 op_sel:[1,0,0]
	v_cvt_scalef32_pk_f16_fp4 v124, v121, 1.0 op_sel:[0,1,0]
	v_cvt_scalef32_pk_f16_fp4 v125, v121, 1.0 op_sel:[1,1,0]
	v_mfma_f32_16x16x32_f16 v[30:33], v[66:69], v[126:129], 0
	v_cvt_scalef32_pk_f16_fp4 v126, v119, 1.0
	v_cvt_scalef32_pk_f16_fp4 v127, v119, 1.0 op_sel:[1,0,0]
	v_cvt_scalef32_pk_f16_fp4 v128, v119, 1.0 op_sel:[0,1,0]
	v_cvt_scalef32_pk_f16_fp4 v129, v119, 1.0 op_sel:[1,1,0]
	v_mfma_f32_16x16x32_f16 v[26:29], v[74:77], v[122:125], v[26:29]
	v_mfma_f32_16x16x32_f16 v[30:33], v[74:77], v[126:129], v[30:33]
	ds_read_b64_tr_b4 v[118:119], v155
	ds_read_b64_tr_b4 v[120:121], v163
	s_waitcnt lgkmcnt(2)
	v_cvt_scalef32_pk_f16_fp4 v122, v114, 1.0
	v_cvt_scalef32_pk_f16_fp4 v123, v114, 1.0 op_sel:[1,0,0]
	v_cvt_scalef32_pk_f16_fp4 v124, v114, 1.0 op_sel:[0,1,0]
	v_cvt_scalef32_pk_f16_fp4 v125, v114, 1.0 op_sel:[1,1,0]
	v_cvt_scalef32_pk_f16_fp4 v126, v116, 1.0
	v_cvt_scalef32_pk_f16_fp4 v127, v116, 1.0 op_sel:[1,0,0]
	v_cvt_scalef32_pk_f16_fp4 v128, v116, 1.0 op_sel:[0,1,0]
	v_cvt_scalef32_pk_f16_fp4 v129, v116, 1.0 op_sel:[1,1,0]
	v_mfma_f32_16x16x32_f16 v[34:37], v[66:69], v[122:125], 0
	v_cvt_scalef32_pk_f16_fp4 v122, v117, 1.0
	v_cvt_scalef32_pk_f16_fp4 v123, v117, 1.0 op_sel:[1,0,0]
	v_cvt_scalef32_pk_f16_fp4 v124, v117, 1.0 op_sel:[0,1,0]
	v_cvt_scalef32_pk_f16_fp4 v125, v117, 1.0 op_sel:[1,1,0]
	v_mfma_f32_16x16x32_f16 v[38:41], v[66:69], v[126:129], 0
	v_cvt_scalef32_pk_f16_fp4 v126, v115, 1.0
	v_cvt_scalef32_pk_f16_fp4 v127, v115, 1.0 op_sel:[1,0,0]
	v_cvt_scalef32_pk_f16_fp4 v128, v115, 1.0 op_sel:[0,1,0]
	v_cvt_scalef32_pk_f16_fp4 v129, v115, 1.0 op_sel:[1,1,0]
	v_mfma_f32_16x16x32_f16 v[34:37], v[74:77], v[122:125], v[34:37]
	v_mfma_f32_16x16x32_f16 v[38:41], v[74:77], v[126:129], v[38:41]
	ds_read_b64_tr_b4 v[114:115], v156
	ds_read_b64_tr_b4 v[116:117], v164
	s_waitcnt lgkmcnt(2)
	v_cvt_scalef32_pk_f16_fp4 v122, v118, 1.0
	v_cvt_scalef32_pk_f16_fp4 v123, v118, 1.0 op_sel:[1,0,0]
	v_cvt_scalef32_pk_f16_fp4 v124, v118, 1.0 op_sel:[0,1,0]
	v_cvt_scalef32_pk_f16_fp4 v125, v118, 1.0 op_sel:[1,1,0]
	v_cvt_scalef32_pk_f16_fp4 v126, v120, 1.0
	v_cvt_scalef32_pk_f16_fp4 v127, v120, 1.0 op_sel:[1,0,0]
	v_cvt_scalef32_pk_f16_fp4 v128, v120, 1.0 op_sel:[0,1,0]
	v_cvt_scalef32_pk_f16_fp4 v129, v120, 1.0 op_sel:[1,1,0]
	v_mfma_f32_16x16x32_f16 v[42:45], v[66:69], v[122:125], 0
	v_cvt_scalef32_pk_f16_fp4 v122, v121, 1.0
	v_cvt_scalef32_pk_f16_fp4 v123, v121, 1.0 op_sel:[1,0,0]
	v_cvt_scalef32_pk_f16_fp4 v124, v121, 1.0 op_sel:[0,1,0]
	v_cvt_scalef32_pk_f16_fp4 v125, v121, 1.0 op_sel:[1,1,0]
	v_mfma_f32_16x16x32_f16 v[46:49], v[66:69], v[126:129], 0
	v_cvt_scalef32_pk_f16_fp4 v126, v119, 1.0
	v_cvt_scalef32_pk_f16_fp4 v127, v119, 1.0 op_sel:[1,0,0]
	v_cvt_scalef32_pk_f16_fp4 v128, v119, 1.0 op_sel:[0,1,0]
	v_cvt_scalef32_pk_f16_fp4 v129, v119, 1.0 op_sel:[1,1,0]
	v_mfma_f32_16x16x32_f16 v[42:45], v[74:77], v[122:125], v[42:45]
	v_mfma_f32_16x16x32_f16 v[46:49], v[74:77], v[126:129], v[46:49]
	ds_read_b64_tr_b4 v[118:119], v157
	ds_read_b64_tr_b4 v[120:121], v165
	s_waitcnt lgkmcnt(2)
	v_cvt_scalef32_pk_f16_fp4 v122, v114, 1.0
	v_cvt_scalef32_pk_f16_fp4 v123, v114, 1.0 op_sel:[1,0,0]
	v_cvt_scalef32_pk_f16_fp4 v124, v114, 1.0 op_sel:[0,1,0]
	v_cvt_scalef32_pk_f16_fp4 v125, v114, 1.0 op_sel:[1,1,0]
	v_cvt_scalef32_pk_f16_fp4 v126, v116, 1.0
	v_cvt_scalef32_pk_f16_fp4 v127, v116, 1.0 op_sel:[1,0,0]
	v_cvt_scalef32_pk_f16_fp4 v128, v116, 1.0 op_sel:[0,1,0]
	v_cvt_scalef32_pk_f16_fp4 v129, v116, 1.0 op_sel:[1,1,0]
	v_mfma_f32_16x16x32_f16 v[50:53], v[66:69], v[122:125], 0
	v_cvt_scalef32_pk_f16_fp4 v122, v117, 1.0
	v_cvt_scalef32_pk_f16_fp4 v123, v117, 1.0 op_sel:[1,0,0]
	v_cvt_scalef32_pk_f16_fp4 v124, v117, 1.0 op_sel:[0,1,0]
	v_cvt_scalef32_pk_f16_fp4 v125, v117, 1.0 op_sel:[1,1,0]
	v_mfma_f32_16x16x32_f16 v[54:57], v[66:69], v[126:129], 0
	v_cvt_scalef32_pk_f16_fp4 v126, v115, 1.0
	v_cvt_scalef32_pk_f16_fp4 v127, v115, 1.0 op_sel:[1,0,0]
	v_cvt_scalef32_pk_f16_fp4 v128, v115, 1.0 op_sel:[0,1,0]
	v_cvt_scalef32_pk_f16_fp4 v129, v115, 1.0 op_sel:[1,1,0]
	v_mfma_f32_16x16x32_f16 v[50:53], v[74:77], v[122:125], v[50:53]
	v_mfma_f32_16x16x32_f16 v[54:57], v[74:77], v[126:129], v[54:57]
	s_waitcnt vmcnt(0)
	ds_read_b64_tr_b4 v[114:115], v150 offset:8192
	ds_read_b64_tr_b4 v[116:117], v158 offset:8192
	s_waitcnt lgkmcnt(2)
	v_cvt_scalef32_pk_f16_fp4 v122, v118, 1.0
	v_cvt_scalef32_pk_f16_fp4 v123, v118, 1.0 op_sel:[1,0,0]
	v_cvt_scalef32_pk_f16_fp4 v124, v118, 1.0 op_sel:[0,1,0]
	v_cvt_scalef32_pk_f16_fp4 v125, v118, 1.0 op_sel:[1,1,0]
	v_cvt_scalef32_pk_f16_fp4 v126, v120, 1.0
	v_cvt_scalef32_pk_f16_fp4 v127, v120, 1.0 op_sel:[1,0,0]
	v_cvt_scalef32_pk_f16_fp4 v128, v120, 1.0 op_sel:[0,1,0]
	v_cvt_scalef32_pk_f16_fp4 v129, v120, 1.0 op_sel:[1,1,0]
	v_mfma_f32_16x16x32_f16 v[58:61], v[66:69], v[122:125], 0
	v_cvt_scalef32_pk_f16_fp4 v122, v121, 1.0
	v_cvt_scalef32_pk_f16_fp4 v123, v121, 1.0 op_sel:[1,0,0]
	v_cvt_scalef32_pk_f16_fp4 v124, v121, 1.0 op_sel:[0,1,0]
	v_cvt_scalef32_pk_f16_fp4 v125, v121, 1.0 op_sel:[1,1,0]
	v_mfma_f32_16x16x32_f16 v[62:65], v[66:69], v[126:129], 0
	v_cvt_scalef32_pk_f16_fp4 v126, v119, 1.0
	v_cvt_scalef32_pk_f16_fp4 v127, v119, 1.0 op_sel:[1,0,0]
	v_cvt_scalef32_pk_f16_fp4 v128, v119, 1.0 op_sel:[0,1,0]
	v_cvt_scalef32_pk_f16_fp4 v129, v119, 1.0 op_sel:[1,1,0]
	v_mfma_f32_16x16x32_f16 v[58:61], v[74:77], v[122:125], v[58:61]
	v_mfma_f32_16x16x32_f16 v[62:65], v[74:77], v[126:129], v[62:65]
	ds_read_b64_tr_b4 v[118:119], v151 offset:8192
	ds_read_b64_tr_b4 v[120:121], v159 offset:8192
	s_waitcnt lgkmcnt(2)
	v_cvt_scalef32_pk_f16_fp4 v122, v114, 1.0
	v_cvt_scalef32_pk_f16_fp4 v123, v114, 1.0 op_sel:[1,0,0]
	v_cvt_scalef32_pk_f16_fp4 v124, v114, 1.0 op_sel:[0,1,0]
	v_cvt_scalef32_pk_f16_fp4 v125, v114, 1.0 op_sel:[1,1,0]
	v_cvt_scalef32_pk_f16_fp4 v126, v116, 1.0
	v_cvt_scalef32_pk_f16_fp4 v127, v116, 1.0 op_sel:[1,0,0]
	v_cvt_scalef32_pk_f16_fp4 v128, v116, 1.0 op_sel:[0,1,0]
	v_cvt_scalef32_pk_f16_fp4 v129, v116, 1.0 op_sel:[1,1,0]
	v_mfma_f32_16x16x32_f16 v[2:5], v[70:73], v[122:125], v[2:5]
	v_cvt_scalef32_pk_f16_fp4 v122, v117, 1.0
	v_cvt_scalef32_pk_f16_fp4 v123, v117, 1.0 op_sel:[1,0,0]
	v_cvt_scalef32_pk_f16_fp4 v124, v117, 1.0 op_sel:[0,1,0]
	v_cvt_scalef32_pk_f16_fp4 v125, v117, 1.0 op_sel:[1,1,0]
	v_mfma_f32_16x16x32_f16 v[6:9], v[70:73], v[126:129], v[6:9]
	v_cvt_scalef32_pk_f16_fp4 v126, v115, 1.0
	v_cvt_scalef32_pk_f16_fp4 v127, v115, 1.0 op_sel:[1,0,0]
	v_cvt_scalef32_pk_f16_fp4 v128, v115, 1.0 op_sel:[0,1,0]
	v_cvt_scalef32_pk_f16_fp4 v129, v115, 1.0 op_sel:[1,1,0]
	v_mfma_f32_16x16x32_f16 v[2:5], v[78:81], v[122:125], v[2:5]
	v_mfma_f32_16x16x32_f16 v[6:9], v[78:81], v[126:129], v[6:9]
	ds_read_b64_tr_b4 v[114:115], v152 offset:8192
	ds_read_b64_tr_b4 v[116:117], v160 offset:8192
	s_waitcnt lgkmcnt(2)
	s_add_i32 m0, s38, 0x0
	v_mad_u32_u16 v178, v106, v198, v166
	global_load_lds_dwordx4 v178, s[40:41]
	s_add_i32 m0, s38, 0x400
	v_mad_u32_u16 v179, v106, v198, v167 op_sel:[1,0,0,0]
	global_load_lds_dwordx4 v179, s[40:41]
	s_add_i32 m0, s38, 0x800
	v_mad_u32_u16 v178, v107, v198, v168
	global_load_lds_dwordx4 v178, s[40:41]
	s_add_i32 m0, s38, 0xc00
	v_mad_u32_u16 v179, v107, v198, v169 op_sel:[1,0,0,0]
	global_load_lds_dwordx4 v179, s[40:41]
	s_add_i32 m0, s38, 0x1000
	v_mad_u32_u16 v178, v108, v198, v170
	global_load_lds_dwordx4 v178, s[40:41]
	s_add_i32 m0, s38, 0x1400
	v_mad_u32_u16 v179, v108, v198, v171 op_sel:[1,0,0,0]
	global_load_lds_dwordx4 v179, s[40:41]
	s_add_i32 m0, s38, 0x1800
	v_mad_u32_u16 v178, v109, v198, v172
	global_load_lds_dwordx4 v178, s[40:41]
	s_add_i32 m0, s38, 0x1c00
	v_mad_u32_u16 v179, v109, v198, v173 op_sel:[1,0,0,0]
	global_load_lds_dwordx4 v179, s[40:41]
	v_cvt_scalef32_pk_f16_fp4 v122, v118, 1.0
	v_cvt_scalef32_pk_f16_fp4 v123, v118, 1.0 op_sel:[1,0,0]
	v_cvt_scalef32_pk_f16_fp4 v124, v118, 1.0 op_sel:[0,1,0]
	v_cvt_scalef32_pk_f16_fp4 v125, v118, 1.0 op_sel:[1,1,0]
	v_cvt_scalef32_pk_f16_fp4 v126, v120, 1.0
	v_cvt_scalef32_pk_f16_fp4 v127, v120, 1.0 op_sel:[1,0,0]
	v_cvt_scalef32_pk_f16_fp4 v128, v120, 1.0 op_sel:[0,1,0]
	v_cvt_scalef32_pk_f16_fp4 v129, v120, 1.0 op_sel:[1,1,0]
	v_mfma_f32_16x16x32_f16 v[10:13], v[70:73], v[122:125], v[10:13]
	v_cvt_scalef32_pk_f16_fp4 v122, v121, 1.0
	v_cvt_scalef32_pk_f16_fp4 v123, v121, 1.0 op_sel:[1,0,0]
	v_cvt_scalef32_pk_f16_fp4 v124, v121, 1.0 op_sel:[0,1,0]
	v_cvt_scalef32_pk_f16_fp4 v125, v121, 1.0 op_sel:[1,1,0]
	v_mfma_f32_16x16x32_f16 v[14:17], v[70:73], v[126:129], v[14:17]
	v_cvt_scalef32_pk_f16_fp4 v126, v119, 1.0
	v_cvt_scalef32_pk_f16_fp4 v127, v119, 1.0 op_sel:[1,0,0]
	v_cvt_scalef32_pk_f16_fp4 v128, v119, 1.0 op_sel:[0,1,0]
	v_cvt_scalef32_pk_f16_fp4 v129, v119, 1.0 op_sel:[1,1,0]
	v_mfma_f32_16x16x32_f16 v[10:13], v[78:81], v[122:125], v[10:13]
	v_mfma_f32_16x16x32_f16 v[14:17], v[78:81], v[126:129], v[14:17]
	ds_read_b64_tr_b4 v[118:119], v153 offset:8192
	ds_read_b64_tr_b4 v[120:121], v161 offset:8192
	s_waitcnt lgkmcnt(2)
	v_cvt_scalef32_pk_f16_fp4 v122, v114, 1.0
	v_cvt_scalef32_pk_f16_fp4 v123, v114, 1.0 op_sel:[1,0,0]
	v_cvt_scalef32_pk_f16_fp4 v124, v114, 1.0 op_sel:[0,1,0]
	v_cvt_scalef32_pk_f16_fp4 v125, v114, 1.0 op_sel:[1,1,0]
	v_cvt_scalef32_pk_f16_fp4 v126, v116, 1.0
	v_cvt_scalef32_pk_f16_fp4 v127, v116, 1.0 op_sel:[1,0,0]
	v_cvt_scalef32_pk_f16_fp4 v128, v116, 1.0 op_sel:[0,1,0]
	v_cvt_scalef32_pk_f16_fp4 v129, v116, 1.0 op_sel:[1,1,0]
	v_mfma_f32_16x16x32_f16 v[18:21], v[70:73], v[122:125], v[18:21]
	v_cvt_scalef32_pk_f16_fp4 v122, v117, 1.0
	v_cvt_scalef32_pk_f16_fp4 v123, v117, 1.0 op_sel:[1,0,0]
	v_cvt_scalef32_pk_f16_fp4 v124, v117, 1.0 op_sel:[0,1,0]
	v_cvt_scalef32_pk_f16_fp4 v125, v117, 1.0 op_sel:[1,1,0]
	v_mfma_f32_16x16x32_f16 v[22:25], v[70:73], v[126:129], v[22:25]
	v_cvt_scalef32_pk_f16_fp4 v126, v115, 1.0
	v_cvt_scalef32_pk_f16_fp4 v127, v115, 1.0 op_sel:[1,0,0]
	v_cvt_scalef32_pk_f16_fp4 v128, v115, 1.0 op_sel:[0,1,0]
	v_cvt_scalef32_pk_f16_fp4 v129, v115, 1.0 op_sel:[1,1,0]
	v_mfma_f32_16x16x32_f16 v[18:21], v[78:81], v[122:125], v[18:21]
	v_mfma_f32_16x16x32_f16 v[22:25], v[78:81], v[126:129], v[22:25]
	ds_read_b64_tr_b4 v[114:115], v154 offset:8192
	ds_read_b64_tr_b4 v[116:117], v162 offset:8192
	s_waitcnt lgkmcnt(2)
	v_cvt_scalef32_pk_f16_fp4 v122, v118, 1.0
	v_cvt_scalef32_pk_f16_fp4 v123, v118, 1.0 op_sel:[1,0,0]
	v_cvt_scalef32_pk_f16_fp4 v124, v118, 1.0 op_sel:[0,1,0]
	v_cvt_scalef32_pk_f16_fp4 v125, v118, 1.0 op_sel:[1,1,0]
	v_cvt_scalef32_pk_f16_fp4 v126, v120, 1.0
	v_cvt_scalef32_pk_f16_fp4 v127, v120, 1.0 op_sel:[1,0,0]
	v_cvt_scalef32_pk_f16_fp4 v128, v120, 1.0 op_sel:[0,1,0]
	v_cvt_scalef32_pk_f16_fp4 v129, v120, 1.0 op_sel:[1,1,0]
	v_mfma_f32_16x16x32_f16 v[26:29], v[70:73], v[122:125], v[26:29]
	v_cvt_scalef32_pk_f16_fp4 v122, v121, 1.0
	v_cvt_scalef32_pk_f16_fp4 v123, v121, 1.0 op_sel:[1,0,0]
	v_cvt_scalef32_pk_f16_fp4 v124, v121, 1.0 op_sel:[0,1,0]
	v_cvt_scalef32_pk_f16_fp4 v125, v121, 1.0 op_sel:[1,1,0]
	v_mfma_f32_16x16x32_f16 v[30:33], v[70:73], v[126:129], v[30:33]
	v_cvt_scalef32_pk_f16_fp4 v126, v119, 1.0
	v_cvt_scalef32_pk_f16_fp4 v127, v119, 1.0 op_sel:[1,0,0]
	v_cvt_scalef32_pk_f16_fp4 v128, v119, 1.0 op_sel:[0,1,0]
	v_cvt_scalef32_pk_f16_fp4 v129, v119, 1.0 op_sel:[1,1,0]
	v_mfma_f32_16x16x32_f16 v[26:29], v[78:81], v[122:125], v[26:29]
	v_mfma_f32_16x16x32_f16 v[30:33], v[78:81], v[126:129], v[30:33]
	ds_read_b64_tr_b4 v[118:119], v155 offset:8192
	ds_read_b64_tr_b4 v[120:121], v163 offset:8192
	s_waitcnt lgkmcnt(2)
	v_cvt_scalef32_pk_f16_fp4 v122, v114, 1.0
	v_cvt_scalef32_pk_f16_fp4 v123, v114, 1.0 op_sel:[1,0,0]
	v_cvt_scalef32_pk_f16_fp4 v124, v114, 1.0 op_sel:[0,1,0]
	v_cvt_scalef32_pk_f16_fp4 v125, v114, 1.0 op_sel:[1,1,0]
	v_cvt_scalef32_pk_f16_fp4 v126, v116, 1.0
	v_cvt_scalef32_pk_f16_fp4 v127, v116, 1.0 op_sel:[1,0,0]
	v_cvt_scalef32_pk_f16_fp4 v128, v116, 1.0 op_sel:[0,1,0]
	v_cvt_scalef32_pk_f16_fp4 v129, v116, 1.0 op_sel:[1,1,0]
	v_mfma_f32_16x16x32_f16 v[34:37], v[70:73], v[122:125], v[34:37]
	v_cvt_scalef32_pk_f16_fp4 v122, v117, 1.0
	v_cvt_scalef32_pk_f16_fp4 v123, v117, 1.0 op_sel:[1,0,0]
	v_cvt_scalef32_pk_f16_fp4 v124, v117, 1.0 op_sel:[0,1,0]
	v_cvt_scalef32_pk_f16_fp4 v125, v117, 1.0 op_sel:[1,1,0]
	v_mfma_f32_16x16x32_f16 v[38:41], v[70:73], v[126:129], v[38:41]
	v_cvt_scalef32_pk_f16_fp4 v126, v115, 1.0
	v_cvt_scalef32_pk_f16_fp4 v127, v115, 1.0 op_sel:[1,0,0]
	v_cvt_scalef32_pk_f16_fp4 v128, v115, 1.0 op_sel:[0,1,0]
	v_cvt_scalef32_pk_f16_fp4 v129, v115, 1.0 op_sel:[1,1,0]
	v_mfma_f32_16x16x32_f16 v[34:37], v[78:81], v[122:125], v[34:37]
	v_mfma_f32_16x16x32_f16 v[38:41], v[78:81], v[126:129], v[38:41]
	ds_read_b64_tr_b4 v[114:115], v156 offset:8192
	ds_read_b64_tr_b4 v[116:117], v164 offset:8192
	s_waitcnt lgkmcnt(2)
	v_cvt_scalef32_pk_f16_fp4 v122, v118, 1.0
	v_cvt_scalef32_pk_f16_fp4 v123, v118, 1.0 op_sel:[1,0,0]
	v_cvt_scalef32_pk_f16_fp4 v124, v118, 1.0 op_sel:[0,1,0]
	v_cvt_scalef32_pk_f16_fp4 v125, v118, 1.0 op_sel:[1,1,0]
	v_cvt_scalef32_pk_f16_fp4 v126, v120, 1.0
	v_cvt_scalef32_pk_f16_fp4 v127, v120, 1.0 op_sel:[1,0,0]
	v_cvt_scalef32_pk_f16_fp4 v128, v120, 1.0 op_sel:[0,1,0]
	v_cvt_scalef32_pk_f16_fp4 v129, v120, 1.0 op_sel:[1,1,0]
	v_mfma_f32_16x16x32_f16 v[42:45], v[70:73], v[122:125], v[42:45]
	v_cvt_scalef32_pk_f16_fp4 v122, v121, 1.0
	v_cvt_scalef32_pk_f16_fp4 v123, v121, 1.0 op_sel:[1,0,0]
	v_cvt_scalef32_pk_f16_fp4 v124, v121, 1.0 op_sel:[0,1,0]
	v_cvt_scalef32_pk_f16_fp4 v125, v121, 1.0 op_sel:[1,1,0]
	v_mfma_f32_16x16x32_f16 v[46:49], v[70:73], v[126:129], v[46:49]
	v_cvt_scalef32_pk_f16_fp4 v126, v119, 1.0
	v_cvt_scalef32_pk_f16_fp4 v127, v119, 1.0 op_sel:[1,0,0]
	v_cvt_scalef32_pk_f16_fp4 v128, v119, 1.0 op_sel:[0,1,0]
	v_cvt_scalef32_pk_f16_fp4 v129, v119, 1.0 op_sel:[1,1,0]
	v_mfma_f32_16x16x32_f16 v[42:45], v[78:81], v[122:125], v[42:45]
	v_mfma_f32_16x16x32_f16 v[46:49], v[78:81], v[126:129], v[46:49]
	ds_read_b64_tr_b4 v[118:119], v157 offset:8192
	ds_read_b64_tr_b4 v[120:121], v165 offset:8192
	s_waitcnt lgkmcnt(2)
	v_cvt_scalef32_pk_f16_fp4 v122, v114, 1.0
	v_cvt_scalef32_pk_f16_fp4 v123, v114, 1.0 op_sel:[1,0,0]
	v_cvt_scalef32_pk_f16_fp4 v124, v114, 1.0 op_sel:[0,1,0]
	v_cvt_scalef32_pk_f16_fp4 v125, v114, 1.0 op_sel:[1,1,0]
	v_cvt_scalef32_pk_f16_fp4 v126, v116, 1.0
	v_cvt_scalef32_pk_f16_fp4 v127, v116, 1.0 op_sel:[1,0,0]
	v_cvt_scalef32_pk_f16_fp4 v128, v116, 1.0 op_sel:[0,1,0]
	v_cvt_scalef32_pk_f16_fp4 v129, v116, 1.0 op_sel:[1,1,0]
	v_mfma_f32_16x16x32_f16 v[50:53], v[70:73], v[122:125], v[50:53]
	v_cvt_scalef32_pk_f16_fp4 v122, v117, 1.0
	v_cvt_scalef32_pk_f16_fp4 v123, v117, 1.0 op_sel:[1,0,0]
	v_cvt_scalef32_pk_f16_fp4 v124, v117, 1.0 op_sel:[0,1,0]
	v_cvt_scalef32_pk_f16_fp4 v125, v117, 1.0 op_sel:[1,1,0]
	v_mfma_f32_16x16x32_f16 v[54:57], v[70:73], v[126:129], v[54:57]
	v_cvt_scalef32_pk_f16_fp4 v126, v115, 1.0
	v_cvt_scalef32_pk_f16_fp4 v127, v115, 1.0 op_sel:[1,0,0]
	v_cvt_scalef32_pk_f16_fp4 v128, v115, 1.0 op_sel:[0,1,0]
	v_cvt_scalef32_pk_f16_fp4 v129, v115, 1.0 op_sel:[1,1,0]
	v_mfma_f32_16x16x32_f16 v[50:53], v[78:81], v[122:125], v[50:53]
	v_mfma_f32_16x16x32_f16 v[54:57], v[78:81], v[126:129], v[54:57]
	s_waitcnt vmcnt(0)
	ds_read_b64_tr_b4 v[114:115], v150
	ds_read_b64_tr_b4 v[116:117], v158
	s_waitcnt lgkmcnt(2)
	ds_read_b128 v[82:85], v174 offset:256
	ds_read_b128 v[86:89], v174 offset:272
	ds_read_b128 v[90:93], v175 offset:256
	ds_read_b128 v[94:97], v175 offset:272
	ds_read_b128 v[98:101], v199
	ds_read_b128 v[102:105], v199 offset:16
	v_cvt_scalef32_pk_f16_fp4 v122, v118, 1.0
	v_cvt_scalef32_pk_f16_fp4 v123, v118, 1.0 op_sel:[1,0,0]
	v_cvt_scalef32_pk_f16_fp4 v124, v118, 1.0 op_sel:[0,1,0]
	v_cvt_scalef32_pk_f16_fp4 v125, v118, 1.0 op_sel:[1,1,0]
	v_cvt_scalef32_pk_f16_fp4 v126, v120, 1.0
	v_cvt_scalef32_pk_f16_fp4 v127, v120, 1.0 op_sel:[1,0,0]
	v_cvt_scalef32_pk_f16_fp4 v128, v120, 1.0 op_sel:[0,1,0]
	v_cvt_scalef32_pk_f16_fp4 v129, v120, 1.0 op_sel:[1,1,0]
	v_mfma_f32_16x16x32_f16 v[58:61], v[70:73], v[122:125], v[58:61]
	v_cvt_scalef32_pk_f16_fp4 v122, v121, 1.0
	v_cvt_scalef32_pk_f16_fp4 v123, v121, 1.0 op_sel:[1,0,0]
	v_cvt_scalef32_pk_f16_fp4 v124, v121, 1.0 op_sel:[0,1,0]
	v_cvt_scalef32_pk_f16_fp4 v125, v121, 1.0 op_sel:[1,1,0]
	v_mfma_f32_16x16x32_f16 v[62:65], v[70:73], v[126:129], v[62:65]
	v_cvt_scalef32_pk_f16_fp4 v126, v119, 1.0
	v_cvt_scalef32_pk_f16_fp4 v127, v119, 1.0 op_sel:[1,0,0]
	v_cvt_scalef32_pk_f16_fp4 v128, v119, 1.0 op_sel:[0,1,0]
	v_cvt_scalef32_pk_f16_fp4 v129, v119, 1.0 op_sel:[1,1,0]
	v_mfma_f32_16x16x32_f16 v[58:61], v[78:81], v[122:125], v[58:61]
	v_mfma_f32_16x16x32_f16 v[62:65], v[78:81], v[126:129], v[62:65]
	s_nop 7
	s_nop 7
	v_cmp_ne_u32_e32 vcc, 0, v196
	v_cndmask_b32_e32 v146, v2, v6, vcc
	v_cndmask_b32_e32 v142, v10, v14, vcc
	v_cndmask_b32_e32 v147, v18, v22, vcc
	v_cndmask_b32_e32 v143, v26, v30, vcc
	v_cndmask_b32_e32 v148, v34, v38, vcc
	v_cndmask_b32_e32 v144, v42, v46, vcc
	v_cndmask_b32_e32 v149, v50, v54, vcc
	v_cndmask_b32_e32 v145, v58, v62, vcc
	v_cmp_ne_u32_e32 vcc, 0, v197
	v_cndmask_b32_e32 v146, v146, v142, vcc
	v_cndmask_b32_e32 v147, v147, v143, vcc
	v_cndmask_b32_e32 v148, v148, v144, vcc
	v_cndmask_b32_e32 v149, v149, v145, vcc
	v_fma_f32 v142, v134, v146, v130
	v_fma_f32 v143, v135, v147, v131
	v_fma_f32 v144, v136, v148, v132
	v_fma_f32 v145, v137, v149, v133
	global_store_dword v[180:181], v142, off
	global_store_dword v[180:181], v143, off offset:256
	global_store_dword v[180:181], v144, off offset:512
	global_store_dword v[180:181], v145, off offset:768
	v_lshl_add_u64 v[180:181], v[180:181], 0, s[48:49]
	s_lshr_b32 s99, s38, 4
	s_add_i32 m0, s99, 0x21000
	s_mov_b64 exec, 0xffff
	global_load_lds_dwordx4 v177, s[0:1]
	s_mov_b64 exec, -1
	v_add_u32_e32 v177, 0x100, v177
	s_lshr_b32 s99, s38, 5
	s_add_i32 m0, s99, 0x23100
	s_mov_b64 exec, 0xffff
	global_load_lds_dwordx4 v176, s[22:23]
	s_mov_b64 exec, -1
	s_lshl_b32 s99, s43, 8
	s_cmp_eq_u32 s33, 4
	s_cselect_b32 s99, s99, 0x100
	v_add_u32_e32 v176, s99, v176
	global_load_dword v130, v[180:181], off
	global_load_dword v131, v[180:181], off offset:256
	global_load_dword v132, v[180:181], off offset:512
	global_load_dword v133, v[180:181], off offset:768
	ds_read_b64_tr_b4 v[118:119], v151
	ds_read_b64_tr_b4 v[120:121], v159
	s_waitcnt lgkmcnt(2)
	v_cvt_scalef32_pk_f16_fp4 v122, v114, 1.0
	v_cvt_scalef32_pk_f16_fp4 v123, v114, 1.0 op_sel:[1,0,0]
	v_cvt_scalef32_pk_f16_fp4 v124, v114, 1.0 op_sel:[0,1,0]
	v_cvt_scalef32_pk_f16_fp4 v125, v114, 1.0 op_sel:[1,1,0]
	v_cvt_scalef32_pk_f16_fp4 v126, v116, 1.0
	v_cvt_scalef32_pk_f16_fp4 v127, v116, 1.0 op_sel:[1,0,0]
	v_cvt_scalef32_pk_f16_fp4 v128, v116, 1.0 op_sel:[0,1,0]
	v_cvt_scalef32_pk_f16_fp4 v129, v116, 1.0 op_sel:[1,1,0]
	v_mfma_f32_16x16x32_f16 v[2:5], v[82:85], v[122:125], 0
	v_cvt_scalef32_pk_f16_fp4 v122, v117, 1.0
	v_cvt_scalef32_pk_f16_fp4 v123, v117, 1.0 op_sel:[1,0,0]
	v_cvt_scalef32_pk_f16_fp4 v124, v117, 1.0 op_sel:[0,1,0]
	v_cvt_scalef32_pk_f16_fp4 v125, v117, 1.0 op_sel:[1,1,0]
	v_mfma_f32_16x16x32_f16 v[6:9], v[82:85], v[126:129], 0
	v_cvt_scalef32_pk_f16_fp4 v126, v115, 1.0
	v_cvt_scalef32_pk_f16_fp4 v127, v115, 1.0 op_sel:[1,0,0]
	v_cvt_scalef32_pk_f16_fp4 v128, v115, 1.0 op_sel:[0,1,0]
	v_cvt_scalef32_pk_f16_fp4 v129, v115, 1.0 op_sel:[1,1,0]
	v_mfma_f32_16x16x32_f16 v[2:5], v[90:93], v[122:125], v[2:5]
	v_mfma_f32_16x16x32_f16 v[6:9], v[90:93], v[126:129], v[6:9]
	ds_read_b64_tr_b4 v[114:115], v152
	ds_read_b64_tr_b4 v[116:117], v160
	s_waitcnt lgkmcnt(2)
	s_add_i32 m0, s38, 0x2000
	v_mad_u32_u16 v178, v110, v198, v166
	global_load_lds_dwordx4 v178, s[40:41]
	s_add_i32 m0, s38, 0x2400
	v_mad_u32_u16 v179, v110, v198, v167 op_sel:[1,0,0,0]
	global_load_lds_dwordx4 v179, s[40:41]
	s_add_i32 m0, s38, 0x2800
	v_mad_u32_u16 v178, v111, v198, v168
	global_load_lds_dwordx4 v178, s[40:41]
	s_add_i32 m0, s38, 0x2c00
	v_mad_u32_u16 v179, v111, v198, v169 op_sel:[1,0,0,0]
	global_load_lds_dwordx4 v179, s[40:41]
	s_add_i32 m0, s38, 0x3000
	v_mad_u32_u16 v178, v112, v198, v170
	global_load_lds_dwordx4 v178, s[40:41]
	s_add_i32 m0, s38, 0x3400
	v_mad_u32_u16 v179, v112, v198, v171 op_sel:[1,0,0,0]
	global_load_lds_dwordx4 v179, s[40:41]
	s_add_i32 m0, s38, 0x3800
	v_mad_u32_u16 v178, v113, v198, v172
	global_load_lds_dwordx4 v178, s[40:41]
	s_add_i32 m0, s38, 0x3c00
	v_mad_u32_u16 v179, v113, v198, v173 op_sel:[1,0,0,0]
	global_load_lds_dwordx4 v179, s[40:41]
	v_cvt_scalef32_pk_f16_fp4 v122, v118, 1.0
	v_cvt_scalef32_pk_f16_fp4 v123, v118, 1.0 op_sel:[1,0,0]
	v_cvt_scalef32_pk_f16_fp4 v124, v118, 1.0 op_sel:[0,1,0]
	v_cvt_scalef32_pk_f16_fp4 v125, v118, 1.0 op_sel:[1,1,0]
	v_cvt_scalef32_pk_f16_fp4 v126, v120, 1.0
	v_cvt_scalef32_pk_f16_fp4 v127, v120, 1.0 op_sel:[1,0,0]
	v_cvt_scalef32_pk_f16_fp4 v128, v120, 1.0 op_sel:[0,1,0]
	v_cvt_scalef32_pk_f16_fp4 v129, v120, 1.0 op_sel:[1,1,0]
	v_mfma_f32_16x16x32_f16 v[10:13], v[82:85], v[122:125], 0
	v_cvt_scalef32_pk_f16_fp4 v122, v121, 1.0
	v_cvt_scalef32_pk_f16_fp4 v123, v121, 1.0 op_sel:[1,0,0]
	v_cvt_scalef32_pk_f16_fp4 v124, v121, 1.0 op_sel:[0,1,0]
	v_cvt_scalef32_pk_f16_fp4 v125, v121, 1.0 op_sel:[1,1,0]
	v_mfma_f32_16x16x32_f16 v[14:17], v[82:85], v[126:129], 0
	v_cvt_scalef32_pk_f16_fp4 v126, v119, 1.0
	v_cvt_scalef32_pk_f16_fp4 v127, v119, 1.0 op_sel:[1,0,0]
	v_cvt_scalef32_pk_f16_fp4 v128, v119, 1.0 op_sel:[0,1,0]
	v_cvt_scalef32_pk_f16_fp4 v129, v119, 1.0 op_sel:[1,1,0]
	v_mfma_f32_16x16x32_f16 v[10:13], v[90:93], v[122:125], v[10:13]
	v_mfma_f32_16x16x32_f16 v[14:17], v[90:93], v[126:129], v[14:17]
	ds_read_b64_tr_b4 v[118:119], v153
	ds_read_b64_tr_b4 v[120:121], v161
	s_waitcnt lgkmcnt(2)
	v_cvt_scalef32_pk_f16_fp4 v122, v114, 1.0
	v_cvt_scalef32_pk_f16_fp4 v123, v114, 1.0 op_sel:[1,0,0]
	v_cvt_scalef32_pk_f16_fp4 v124, v114, 1.0 op_sel:[0,1,0]
	v_cvt_scalef32_pk_f16_fp4 v125, v114, 1.0 op_sel:[1,1,0]
	v_cvt_scalef32_pk_f16_fp4 v126, v116, 1.0
	v_cvt_scalef32_pk_f16_fp4 v127, v116, 1.0 op_sel:[1,0,0]
	v_cvt_scalef32_pk_f16_fp4 v128, v116, 1.0 op_sel:[0,1,0]
	v_cvt_scalef32_pk_f16_fp4 v129, v116, 1.0 op_sel:[1,1,0]
	v_mfma_f32_16x16x32_f16 v[18:21], v[82:85], v[122:125], 0
	v_cvt_scalef32_pk_f16_fp4 v122, v117, 1.0
	v_cvt_scalef32_pk_f16_fp4 v123, v117, 1.0 op_sel:[1,0,0]
	v_cvt_scalef32_pk_f16_fp4 v124, v117, 1.0 op_sel:[0,1,0]
	v_cvt_scalef32_pk_f16_fp4 v125, v117, 1.0 op_sel:[1,1,0]
	v_mfma_f32_16x16x32_f16 v[22:25], v[82:85], v[126:129], 0
	v_cvt_scalef32_pk_f16_fp4 v126, v115, 1.0
	v_cvt_scalef32_pk_f16_fp4 v127, v115, 1.0 op_sel:[1,0,0]
	v_cvt_scalef32_pk_f16_fp4 v128, v115, 1.0 op_sel:[0,1,0]
	v_cvt_scalef32_pk_f16_fp4 v129, v115, 1.0 op_sel:[1,1,0]
	v_mfma_f32_16x16x32_f16 v[18:21], v[90:93], v[122:125], v[18:21]
	v_mfma_f32_16x16x32_f16 v[22:25], v[90:93], v[126:129], v[22:25]
	ds_read_b64_tr_b4 v[114:115], v154
	ds_read_b64_tr_b4 v[116:117], v162
	s_waitcnt lgkmcnt(2)
	v_cvt_scalef32_pk_f16_fp4 v122, v118, 1.0
	v_cvt_scalef32_pk_f16_fp4 v123, v118, 1.0 op_sel:[1,0,0]
	v_cvt_scalef32_pk_f16_fp4 v124, v118, 1.0 op_sel:[0,1,0]
	v_cvt_scalef32_pk_f16_fp4 v125, v118, 1.0 op_sel:[1,1,0]
	v_cvt_scalef32_pk_f16_fp4 v126, v120, 1.0
	v_cvt_scalef32_pk_f16_fp4 v127, v120, 1.0 op_sel:[1,0,0]
	v_cvt_scalef32_pk_f16_fp4 v128, v120, 1.0 op_sel:[0,1,0]
	v_cvt_scalef32_pk_f16_fp4 v129, v120, 1.0 op_sel:[1,1,0]
	v_mfma_f32_16x16x32_f16 v[26:29], v[82:85], v[122:125], 0
	v_cvt_scalef32_pk_f16_fp4 v122, v121, 1.0
	v_cvt_scalef32_pk_f16_fp4 v123, v121, 1.0 op_sel:[1,0,0]
	v_cvt_scalef32_pk_f16_fp4 v124, v121, 1.0 op_sel:[0,1,0]
	v_cvt_scalef32_pk_f16_fp4 v125, v121, 1.0 op_sel:[1,1,0]
	v_mfma_f32_16x16x32_f16 v[30:33], v[82:85], v[126:129], 0
	v_cvt_scalef32_pk_f16_fp4 v126, v119, 1.0
	v_cvt_scalef32_pk_f16_fp4 v127, v119, 1.0 op_sel:[1,0,0]
	v_cvt_scalef32_pk_f16_fp4 v128, v119, 1.0 op_sel:[0,1,0]
	v_cvt_scalef32_pk_f16_fp4 v129, v119, 1.0 op_sel:[1,1,0]
	v_mfma_f32_16x16x32_f16 v[26:29], v[90:93], v[122:125], v[26:29]
	v_mfma_f32_16x16x32_f16 v[30:33], v[90:93], v[126:129], v[30:33]
	ds_read_b64_tr_b4 v[118:119], v155
	ds_read_b64_tr_b4 v[120:121], v163
	s_waitcnt lgkmcnt(2)
	v_cvt_scalef32_pk_f16_fp4 v122, v114, 1.0
	v_cvt_scalef32_pk_f16_fp4 v123, v114, 1.0 op_sel:[1,0,0]
	v_cvt_scalef32_pk_f16_fp4 v124, v114, 1.0 op_sel:[0,1,0]
	v_cvt_scalef32_pk_f16_fp4 v125, v114, 1.0 op_sel:[1,1,0]
	v_cvt_scalef32_pk_f16_fp4 v126, v116, 1.0
	v_cvt_scalef32_pk_f16_fp4 v127, v116, 1.0 op_sel:[1,0,0]
	v_cvt_scalef32_pk_f16_fp4 v128, v116, 1.0 op_sel:[0,1,0]
	v_cvt_scalef32_pk_f16_fp4 v129, v116, 1.0 op_sel:[1,1,0]
	v_mfma_f32_16x16x32_f16 v[34:37], v[82:85], v[122:125], 0
	v_cvt_scalef32_pk_f16_fp4 v122, v117, 1.0
	v_cvt_scalef32_pk_f16_fp4 v123, v117, 1.0 op_sel:[1,0,0]
	v_cvt_scalef32_pk_f16_fp4 v124, v117, 1.0 op_sel:[0,1,0]
	v_cvt_scalef32_pk_f16_fp4 v125, v117, 1.0 op_sel:[1,1,0]
	v_mfma_f32_16x16x32_f16 v[38:41], v[82:85], v[126:129], 0
	v_cvt_scalef32_pk_f16_fp4 v126, v115, 1.0
	v_cvt_scalef32_pk_f16_fp4 v127, v115, 1.0 op_sel:[1,0,0]
	v_cvt_scalef32_pk_f16_fp4 v128, v115, 1.0 op_sel:[0,1,0]
	v_cvt_scalef32_pk_f16_fp4 v129, v115, 1.0 op_sel:[1,1,0]
	v_mfma_f32_16x16x32_f16 v[34:37], v[90:93], v[122:125], v[34:37]
	v_mfma_f32_16x16x32_f16 v[38:41], v[90:93], v[126:129], v[38:41]
	ds_read_b64_tr_b4 v[114:115], v156
	ds_read_b64_tr_b4 v[116:117], v164
	s_waitcnt lgkmcnt(2)
	v_cvt_scalef32_pk_f16_fp4 v122, v118, 1.0
	v_cvt_scalef32_pk_f16_fp4 v123, v118, 1.0 op_sel:[1,0,0]
	v_cvt_scalef32_pk_f16_fp4 v124, v118, 1.0 op_sel:[0,1,0]
	v_cvt_scalef32_pk_f16_fp4 v125, v118, 1.0 op_sel:[1,1,0]
	v_cvt_scalef32_pk_f16_fp4 v126, v120, 1.0
	v_cvt_scalef32_pk_f16_fp4 v127, v120, 1.0 op_sel:[1,0,0]
	v_cvt_scalef32_pk_f16_fp4 v128, v120, 1.0 op_sel:[0,1,0]
	v_cvt_scalef32_pk_f16_fp4 v129, v120, 1.0 op_sel:[1,1,0]
	v_mfma_f32_16x16x32_f16 v[42:45], v[82:85], v[122:125], 0
	v_cvt_scalef32_pk_f16_fp4 v122, v121, 1.0
	v_cvt_scalef32_pk_f16_fp4 v123, v121, 1.0 op_sel:[1,0,0]
	v_cvt_scalef32_pk_f16_fp4 v124, v121, 1.0 op_sel:[0,1,0]
	v_cvt_scalef32_pk_f16_fp4 v125, v121, 1.0 op_sel:[1,1,0]
	v_mfma_f32_16x16x32_f16 v[46:49], v[82:85], v[126:129], 0
	v_cvt_scalef32_pk_f16_fp4 v126, v119, 1.0
	v_cvt_scalef32_pk_f16_fp4 v127, v119, 1.0 op_sel:[1,0,0]
	v_cvt_scalef32_pk_f16_fp4 v128, v119, 1.0 op_sel:[0,1,0]
	v_cvt_scalef32_pk_f16_fp4 v129, v119, 1.0 op_sel:[1,1,0]
	v_mfma_f32_16x16x32_f16 v[42:45], v[90:93], v[122:125], v[42:45]
	v_mfma_f32_16x16x32_f16 v[46:49], v[90:93], v[126:129], v[46:49]
	ds_read_b64_tr_b4 v[118:119], v157
	ds_read_b64_tr_b4 v[120:121], v165
	s_waitcnt lgkmcnt(2)
	v_cvt_scalef32_pk_f16_fp4 v122, v114, 1.0
	v_cvt_scalef32_pk_f16_fp4 v123, v114, 1.0 op_sel:[1,0,0]
	v_cvt_scalef32_pk_f16_fp4 v124, v114, 1.0 op_sel:[0,1,0]
	v_cvt_scalef32_pk_f16_fp4 v125, v114, 1.0 op_sel:[1,1,0]
	v_cvt_scalef32_pk_f16_fp4 v126, v116, 1.0
	v_cvt_scalef32_pk_f16_fp4 v127, v116, 1.0 op_sel:[1,0,0]
	v_cvt_scalef32_pk_f16_fp4 v128, v116, 1.0 op_sel:[0,1,0]
	v_cvt_scalef32_pk_f16_fp4 v129, v116, 1.0 op_sel:[1,1,0]
	v_mfma_f32_16x16x32_f16 v[50:53], v[82:85], v[122:125], 0
	v_cvt_scalef32_pk_f16_fp4 v122, v117, 1.0
	v_cvt_scalef32_pk_f16_fp4 v123, v117, 1.0 op_sel:[1,0,0]
	v_cvt_scalef32_pk_f16_fp4 v124, v117, 1.0 op_sel:[0,1,0]
	v_cvt_scalef32_pk_f16_fp4 v125, v117, 1.0 op_sel:[1,1,0]
	v_mfma_f32_16x16x32_f16 v[54:57], v[82:85], v[126:129], 0
	v_cvt_scalef32_pk_f16_fp4 v126, v115, 1.0
	v_cvt_scalef32_pk_f16_fp4 v127, v115, 1.0 op_sel:[1,0,0]
	v_cvt_scalef32_pk_f16_fp4 v128, v115, 1.0 op_sel:[0,1,0]
	v_cvt_scalef32_pk_f16_fp4 v129, v115, 1.0 op_sel:[1,1,0]
	v_mfma_f32_16x16x32_f16 v[50:53], v[90:93], v[122:125], v[50:53]
	v_mfma_f32_16x16x32_f16 v[54:57], v[90:93], v[126:129], v[54:57]
	s_waitcnt vmcnt(0)
	ds_read_b64_tr_b4 v[114:115], v150 offset:8192
	ds_read_b64_tr_b4 v[116:117], v158 offset:8192
	s_waitcnt lgkmcnt(2)
	v_cvt_scalef32_pk_f16_fp4 v122, v118, 1.0
	v_cvt_scalef32_pk_f16_fp4 v123, v118, 1.0 op_sel:[1,0,0]
	v_cvt_scalef32_pk_f16_fp4 v124, v118, 1.0 op_sel:[0,1,0]
	v_cvt_scalef32_pk_f16_fp4 v125, v118, 1.0 op_sel:[1,1,0]
	v_cvt_scalef32_pk_f16_fp4 v126, v120, 1.0
	v_cvt_scalef32_pk_f16_fp4 v127, v120, 1.0 op_sel:[1,0,0]
	v_cvt_scalef32_pk_f16_fp4 v128, v120, 1.0 op_sel:[0,1,0]
	v_cvt_scalef32_pk_f16_fp4 v129, v120, 1.0 op_sel:[1,1,0]
	v_mfma_f32_16x16x32_f16 v[58:61], v[82:85], v[122:125], 0
	v_cvt_scalef32_pk_f16_fp4 v122, v121, 1.0
	v_cvt_scalef32_pk_f16_fp4 v123, v121, 1.0 op_sel:[1,0,0]
	v_cvt_scalef32_pk_f16_fp4 v124, v121, 1.0 op_sel:[0,1,0]
	v_cvt_scalef32_pk_f16_fp4 v125, v121, 1.0 op_sel:[1,1,0]
	v_mfma_f32_16x16x32_f16 v[62:65], v[82:85], v[126:129], 0
	v_cvt_scalef32_pk_f16_fp4 v126, v119, 1.0
	v_cvt_scalef32_pk_f16_fp4 v127, v119, 1.0 op_sel:[1,0,0]
	v_cvt_scalef32_pk_f16_fp4 v128, v119, 1.0 op_sel:[0,1,0]
	v_cvt_scalef32_pk_f16_fp4 v129, v119, 1.0 op_sel:[1,1,0]
	v_mfma_f32_16x16x32_f16 v[58:61], v[90:93], v[122:125], v[58:61]
	v_mfma_f32_16x16x32_f16 v[62:65], v[90:93], v[126:129], v[62:65]
	ds_read_b64_tr_b4 v[118:119], v151 offset:8192
	ds_read_b64_tr_b4 v[120:121], v159 offset:8192
	s_waitcnt lgkmcnt(2)
	v_cvt_scalef32_pk_f16_fp4 v122, v114, 1.0
	v_cvt_scalef32_pk_f16_fp4 v123, v114, 1.0 op_sel:[1,0,0]
	v_cvt_scalef32_pk_f16_fp4 v124, v114, 1.0 op_sel:[0,1,0]
	v_cvt_scalef32_pk_f16_fp4 v125, v114, 1.0 op_sel:[1,1,0]
	v_cvt_scalef32_pk_f16_fp4 v126, v116, 1.0
	v_cvt_scalef32_pk_f16_fp4 v127, v116, 1.0 op_sel:[1,0,0]
	v_cvt_scalef32_pk_f16_fp4 v128, v116, 1.0 op_sel:[0,1,0]
	v_cvt_scalef32_pk_f16_fp4 v129, v116, 1.0 op_sel:[1,1,0]
	v_mfma_f32_16x16x32_f16 v[2:5], v[86:89], v[122:125], v[2:5]
	v_cvt_scalef32_pk_f16_fp4 v122, v117, 1.0
	v_cvt_scalef32_pk_f16_fp4 v123, v117, 1.0 op_sel:[1,0,0]
	v_cvt_scalef32_pk_f16_fp4 v124, v117, 1.0 op_sel:[0,1,0]
	v_cvt_scalef32_pk_f16_fp4 v125, v117, 1.0 op_sel:[1,1,0]
	v_mfma_f32_16x16x32_f16 v[6:9], v[86:89], v[126:129], v[6:9]
	v_cvt_scalef32_pk_f16_fp4 v126, v115, 1.0
	v_cvt_scalef32_pk_f16_fp4 v127, v115, 1.0 op_sel:[1,0,0]
	v_cvt_scalef32_pk_f16_fp4 v128, v115, 1.0 op_sel:[0,1,0]
	v_cvt_scalef32_pk_f16_fp4 v129, v115, 1.0 op_sel:[1,1,0]
	v_mfma_f32_16x16x32_f16 v[2:5], v[94:97], v[122:125], v[2:5]
	v_mfma_f32_16x16x32_f16 v[6:9], v[94:97], v[126:129], v[6:9]
	ds_read_b64_tr_b4 v[114:115], v152 offset:8192
	ds_read_b64_tr_b4 v[116:117], v160 offset:8192
	s_waitcnt lgkmcnt(2)
	s_add_i32 m0, s38, 0x0
	v_mad_u32_u16 v178, v98, v198, v166
	global_load_lds_dwordx4 v178, s[40:41]
	s_add_i32 m0, s38, 0x400
	v_mad_u32_u16 v179, v98, v198, v167 op_sel:[1,0,0,0]
	global_load_lds_dwordx4 v179, s[40:41]
	s_add_i32 m0, s38, 0x800
	v_mad_u32_u16 v178, v99, v198, v168
	global_load_lds_dwordx4 v178, s[40:41]
	s_add_i32 m0, s38, 0xc00
	v_mad_u32_u16 v179, v99, v198, v169 op_sel:[1,0,0,0]
	global_load_lds_dwordx4 v179, s[40:41]
	s_add_i32 m0, s38, 0x1000
	v_mad_u32_u16 v178, v100, v198, v170
	global_load_lds_dwordx4 v178, s[40:41]
	s_add_i32 m0, s38, 0x1400
	v_mad_u32_u16 v179, v100, v198, v171 op_sel:[1,0,0,0]
	global_load_lds_dwordx4 v179, s[40:41]
	s_add_i32 m0, s38, 0x1800
	v_mad_u32_u16 v178, v101, v198, v172
	global_load_lds_dwordx4 v178, s[40:41]
	s_add_i32 m0, s38, 0x1c00
	v_mad_u32_u16 v179, v101, v198, v173 op_sel:[1,0,0,0]
	global_load_lds_dwordx4 v179, s[40:41]
	v_cvt_scalef32_pk_f16_fp4 v122, v118, 1.0
	v_cvt_scalef32_pk_f16_fp4 v123, v118, 1.0 op_sel:[1,0,0]
	v_cvt_scalef32_pk_f16_fp4 v124, v118, 1.0 op_sel:[0,1,0]
	v_cvt_scalef32_pk_f16_fp4 v125, v118, 1.0 op_sel:[1,1,0]
	v_cvt_scalef32_pk_f16_fp4 v126, v120, 1.0
	v_cvt_scalef32_pk_f16_fp4 v127, v120, 1.0 op_sel:[1,0,0]
	v_cvt_scalef32_pk_f16_fp4 v128, v120, 1.0 op_sel:[0,1,0]
	v_cvt_scalef32_pk_f16_fp4 v129, v120, 1.0 op_sel:[1,1,0]
	v_mfma_f32_16x16x32_f16 v[10:13], v[86:89], v[122:125], v[10:13]
	v_cvt_scalef32_pk_f16_fp4 v122, v121, 1.0
	v_cvt_scalef32_pk_f16_fp4 v123, v121, 1.0 op_sel:[1,0,0]
	v_cvt_scalef32_pk_f16_fp4 v124, v121, 1.0 op_sel:[0,1,0]
	v_cvt_scalef32_pk_f16_fp4 v125, v121, 1.0 op_sel:[1,1,0]
	v_mfma_f32_16x16x32_f16 v[14:17], v[86:89], v[126:129], v[14:17]
	v_cvt_scalef32_pk_f16_fp4 v126, v119, 1.0
	v_cvt_scalef32_pk_f16_fp4 v127, v119, 1.0 op_sel:[1,0,0]
	v_cvt_scalef32_pk_f16_fp4 v128, v119, 1.0 op_sel:[0,1,0]
	v_cvt_scalef32_pk_f16_fp4 v129, v119, 1.0 op_sel:[1,1,0]
	v_mfma_f32_16x16x32_f16 v[10:13], v[94:97], v[122:125], v[10:13]
	v_mfma_f32_16x16x32_f16 v[14:17], v[94:97], v[126:129], v[14:17]
	ds_read_b64_tr_b4 v[118:119], v153 offset:8192
	ds_read_b64_tr_b4 v[120:121], v161 offset:8192
	s_waitcnt lgkmcnt(2)
	v_cvt_scalef32_pk_f16_fp4 v122, v114, 1.0
	v_cvt_scalef32_pk_f16_fp4 v123, v114, 1.0 op_sel:[1,0,0]
	v_cvt_scalef32_pk_f16_fp4 v124, v114, 1.0 op_sel:[0,1,0]
	v_cvt_scalef32_pk_f16_fp4 v125, v114, 1.0 op_sel:[1,1,0]
	v_cvt_scalef32_pk_f16_fp4 v126, v116, 1.0
	v_cvt_scalef32_pk_f16_fp4 v127, v116, 1.0 op_sel:[1,0,0]
	v_cvt_scalef32_pk_f16_fp4 v128, v116, 1.0 op_sel:[0,1,0]
	v_cvt_scalef32_pk_f16_fp4 v129, v116, 1.0 op_sel:[1,1,0]
	v_mfma_f32_16x16x32_f16 v[18:21], v[86:89], v[122:125], v[18:21]
	v_cvt_scalef32_pk_f16_fp4 v122, v117, 1.0
	v_cvt_scalef32_pk_f16_fp4 v123, v117, 1.0 op_sel:[1,0,0]
	v_cvt_scalef32_pk_f16_fp4 v124, v117, 1.0 op_sel:[0,1,0]
	v_cvt_scalef32_pk_f16_fp4 v125, v117, 1.0 op_sel:[1,1,0]
	v_mfma_f32_16x16x32_f16 v[22:25], v[86:89], v[126:129], v[22:25]
	v_cvt_scalef32_pk_f16_fp4 v126, v115, 1.0
	v_cvt_scalef32_pk_f16_fp4 v127, v115, 1.0 op_sel:[1,0,0]
	v_cvt_scalef32_pk_f16_fp4 v128, v115, 1.0 op_sel:[0,1,0]
	v_cvt_scalef32_pk_f16_fp4 v129, v115, 1.0 op_sel:[1,1,0]
	v_mfma_f32_16x16x32_f16 v[18:21], v[94:97], v[122:125], v[18:21]
	v_mfma_f32_16x16x32_f16 v[22:25], v[94:97], v[126:129], v[22:25]
	ds_read_b64_tr_b4 v[114:115], v154 offset:8192
	ds_read_b64_tr_b4 v[116:117], v162 offset:8192
	s_waitcnt lgkmcnt(2)
	v_cvt_scalef32_pk_f16_fp4 v122, v118, 1.0
	v_cvt_scalef32_pk_f16_fp4 v123, v118, 1.0 op_sel:[1,0,0]
	v_cvt_scalef32_pk_f16_fp4 v124, v118, 1.0 op_sel:[0,1,0]
	v_cvt_scalef32_pk_f16_fp4 v125, v118, 1.0 op_sel:[1,1,0]
	v_cvt_scalef32_pk_f16_fp4 v126, v120, 1.0
	v_cvt_scalef32_pk_f16_fp4 v127, v120, 1.0 op_sel:[1,0,0]
	v_cvt_scalef32_pk_f16_fp4 v128, v120, 1.0 op_sel:[0,1,0]
	v_cvt_scalef32_pk_f16_fp4 v129, v120, 1.0 op_sel:[1,1,0]
	v_mfma_f32_16x16x32_f16 v[26:29], v[86:89], v[122:125], v[26:29]
	v_cvt_scalef32_pk_f16_fp4 v122, v121, 1.0
	v_cvt_scalef32_pk_f16_fp4 v123, v121, 1.0 op_sel:[1,0,0]
	v_cvt_scalef32_pk_f16_fp4 v124, v121, 1.0 op_sel:[0,1,0]
	v_cvt_scalef32_pk_f16_fp4 v125, v121, 1.0 op_sel:[1,1,0]
	v_mfma_f32_16x16x32_f16 v[30:33], v[86:89], v[126:129], v[30:33]
	v_cvt_scalef32_pk_f16_fp4 v126, v119, 1.0
	v_cvt_scalef32_pk_f16_fp4 v127, v119, 1.0 op_sel:[1,0,0]
	v_cvt_scalef32_pk_f16_fp4 v128, v119, 1.0 op_sel:[0,1,0]
	v_cvt_scalef32_pk_f16_fp4 v129, v119, 1.0 op_sel:[1,1,0]
	v_mfma_f32_16x16x32_f16 v[26:29], v[94:97], v[122:125], v[26:29]
	v_mfma_f32_16x16x32_f16 v[30:33], v[94:97], v[126:129], v[30:33]
	ds_read_b64_tr_b4 v[118:119], v155 offset:8192
	ds_read_b64_tr_b4 v[120:121], v163 offset:8192
	s_waitcnt lgkmcnt(2)
	v_cvt_scalef32_pk_f16_fp4 v122, v114, 1.0
	v_cvt_scalef32_pk_f16_fp4 v123, v114, 1.0 op_sel:[1,0,0]
	v_cvt_scalef32_pk_f16_fp4 v124, v114, 1.0 op_sel:[0,1,0]
	v_cvt_scalef32_pk_f16_fp4 v125, v114, 1.0 op_sel:[1,1,0]
	v_cvt_scalef32_pk_f16_fp4 v126, v116, 1.0
	v_cvt_scalef32_pk_f16_fp4 v127, v116, 1.0 op_sel:[1,0,0]
	v_cvt_scalef32_pk_f16_fp4 v128, v116, 1.0 op_sel:[0,1,0]
	v_cvt_scalef32_pk_f16_fp4 v129, v116, 1.0 op_sel:[1,1,0]
	v_mfma_f32_16x16x32_f16 v[34:37], v[86:89], v[122:125], v[34:37]
	v_cvt_scalef32_pk_f16_fp4 v122, v117, 1.0
	v_cvt_scalef32_pk_f16_fp4 v123, v117, 1.0 op_sel:[1,0,0]
	v_cvt_scalef32_pk_f16_fp4 v124, v117, 1.0 op_sel:[0,1,0]
	v_cvt_scalef32_pk_f16_fp4 v125, v117, 1.0 op_sel:[1,1,0]
	v_mfma_f32_16x16x32_f16 v[38:41], v[86:89], v[126:129], v[38:41]
	v_cvt_scalef32_pk_f16_fp4 v126, v115, 1.0
	v_cvt_scalef32_pk_f16_fp4 v127, v115, 1.0 op_sel:[1,0,0]
	v_cvt_scalef32_pk_f16_fp4 v128, v115, 1.0 op_sel:[0,1,0]
	v_cvt_scalef32_pk_f16_fp4 v129, v115, 1.0 op_sel:[1,1,0]
	v_mfma_f32_16x16x32_f16 v[34:37], v[94:97], v[122:125], v[34:37]
	v_mfma_f32_16x16x32_f16 v[38:41], v[94:97], v[126:129], v[38:41]
	ds_read_b64_tr_b4 v[114:115], v156 offset:8192
	ds_read_b64_tr_b4 v[116:117], v164 offset:8192
	s_waitcnt lgkmcnt(2)
	v_cvt_scalef32_pk_f16_fp4 v122, v118, 1.0
	v_cvt_scalef32_pk_f16_fp4 v123, v118, 1.0 op_sel:[1,0,0]
	v_cvt_scalef32_pk_f16_fp4 v124, v118, 1.0 op_sel:[0,1,0]
	v_cvt_scalef32_pk_f16_fp4 v125, v118, 1.0 op_sel:[1,1,0]
	v_cvt_scalef32_pk_f16_fp4 v126, v120, 1.0
	v_cvt_scalef32_pk_f16_fp4 v127, v120, 1.0 op_sel:[1,0,0]
	v_cvt_scalef32_pk_f16_fp4 v128, v120, 1.0 op_sel:[0,1,0]
	v_cvt_scalef32_pk_f16_fp4 v129, v120, 1.0 op_sel:[1,1,0]
	v_mfma_f32_16x16x32_f16 v[42:45], v[86:89], v[122:125], v[42:45]
	v_cvt_scalef32_pk_f16_fp4 v122, v121, 1.0
	v_cvt_scalef32_pk_f16_fp4 v123, v121, 1.0 op_sel:[1,0,0]
	v_cvt_scalef32_pk_f16_fp4 v124, v121, 1.0 op_sel:[0,1,0]
	v_cvt_scalef32_pk_f16_fp4 v125, v121, 1.0 op_sel:[1,1,0]
	v_mfma_f32_16x16x32_f16 v[46:49], v[86:89], v[126:129], v[46:49]
	v_cvt_scalef32_pk_f16_fp4 v126, v119, 1.0
	v_cvt_scalef32_pk_f16_fp4 v127, v119, 1.0 op_sel:[1,0,0]
	v_cvt_scalef32_pk_f16_fp4 v128, v119, 1.0 op_sel:[0,1,0]
	v_cvt_scalef32_pk_f16_fp4 v129, v119, 1.0 op_sel:[1,1,0]
	v_mfma_f32_16x16x32_f16 v[42:45], v[94:97], v[122:125], v[42:45]
	v_mfma_f32_16x16x32_f16 v[46:49], v[94:97], v[126:129], v[46:49]
	ds_read_b64_tr_b4 v[118:119], v157 offset:8192
	ds_read_b64_tr_b4 v[120:121], v165 offset:8192
	s_waitcnt lgkmcnt(2)
	v_cvt_scalef32_pk_f16_fp4 v122, v114, 1.0
	v_cvt_scalef32_pk_f16_fp4 v123, v114, 1.0 op_sel:[1,0,0]
	v_cvt_scalef32_pk_f16_fp4 v124, v114, 1.0 op_sel:[0,1,0]
	v_cvt_scalef32_pk_f16_fp4 v125, v114, 1.0 op_sel:[1,1,0]
	v_cvt_scalef32_pk_f16_fp4 v126, v116, 1.0
	v_cvt_scalef32_pk_f16_fp4 v127, v116, 1.0 op_sel:[1,0,0]
	v_cvt_scalef32_pk_f16_fp4 v128, v116, 1.0 op_sel:[0,1,0]
	v_cvt_scalef32_pk_f16_fp4 v129, v116, 1.0 op_sel:[1,1,0]
	v_mfma_f32_16x16x32_f16 v[50:53], v[86:89], v[122:125], v[50:53]
	v_cvt_scalef32_pk_f16_fp4 v122, v117, 1.0
	v_cvt_scalef32_pk_f16_fp4 v123, v117, 1.0 op_sel:[1,0,0]
	v_cvt_scalef32_pk_f16_fp4 v124, v117, 1.0 op_sel:[0,1,0]
	v_cvt_scalef32_pk_f16_fp4 v125, v117, 1.0 op_sel:[1,1,0]
	v_mfma_f32_16x16x32_f16 v[54:57], v[86:89], v[126:129], v[54:57]
	v_cvt_scalef32_pk_f16_fp4 v126, v115, 1.0
	v_cvt_scalef32_pk_f16_fp4 v127, v115, 1.0 op_sel:[1,0,0]
	v_cvt_scalef32_pk_f16_fp4 v128, v115, 1.0 op_sel:[0,1,0]
	v_cvt_scalef32_pk_f16_fp4 v129, v115, 1.0 op_sel:[1,1,0]
	v_mfma_f32_16x16x32_f16 v[50:53], v[94:97], v[122:125], v[50:53]
	v_mfma_f32_16x16x32_f16 v[54:57], v[94:97], v[126:129], v[54:57]
	s_waitcnt vmcnt(0)
	ds_read_b64_tr_b4 v[114:115], v150
	ds_read_b64_tr_b4 v[116:117], v158
	s_waitcnt lgkmcnt(2)
	ds_read_b128 v[66:69], v174
	ds_read_b128 v[70:73], v174 offset:16
	ds_read_b128 v[74:77], v175
	ds_read_b128 v[78:81], v175 offset:16
	ds_read_b128 v[106:109], v199 offset:256
	ds_read_b128 v[110:113], v199 offset:272
	v_cvt_scalef32_pk_f16_fp4 v122, v118, 1.0
	v_cvt_scalef32_pk_f16_fp4 v123, v118, 1.0 op_sel:[1,0,0]
	v_cvt_scalef32_pk_f16_fp4 v124, v118, 1.0 op_sel:[0,1,0]
	v_cvt_scalef32_pk_f16_fp4 v125, v118, 1.0 op_sel:[1,1,0]
	v_cvt_scalef32_pk_f16_fp4 v126, v120, 1.0
	v_cvt_scalef32_pk_f16_fp4 v127, v120, 1.0 op_sel:[1,0,0]
	v_cvt_scalef32_pk_f16_fp4 v128, v120, 1.0 op_sel:[0,1,0]
	v_cvt_scalef32_pk_f16_fp4 v129, v120, 1.0 op_sel:[1,1,0]
	v_mfma_f32_16x16x32_f16 v[58:61], v[86:89], v[122:125], v[58:61]
	v_cvt_scalef32_pk_f16_fp4 v122, v121, 1.0
	v_cvt_scalef32_pk_f16_fp4 v123, v121, 1.0 op_sel:[1,0,0]
	v_cvt_scalef32_pk_f16_fp4 v124, v121, 1.0 op_sel:[0,1,0]
	v_cvt_scalef32_pk_f16_fp4 v125, v121, 1.0 op_sel:[1,1,0]
	v_mfma_f32_16x16x32_f16 v[62:65], v[86:89], v[126:129], v[62:65]
	v_cvt_scalef32_pk_f16_fp4 v126, v119, 1.0
	v_cvt_scalef32_pk_f16_fp4 v127, v119, 1.0 op_sel:[1,0,0]
	v_cvt_scalef32_pk_f16_fp4 v128, v119, 1.0 op_sel:[0,1,0]
	v_cvt_scalef32_pk_f16_fp4 v129, v119, 1.0 op_sel:[1,1,0]
	v_mfma_f32_16x16x32_f16 v[58:61], v[94:97], v[122:125], v[58:61]
	v_mfma_f32_16x16x32_f16 v[62:65], v[94:97], v[126:129], v[62:65]
	s_nop 7
	s_nop 7
	v_cmp_ne_u32_e32 vcc, 0, v196
	v_cndmask_b32_e32 v146, v2, v6, vcc
	v_cndmask_b32_e32 v142, v10, v14, vcc
	v_cndmask_b32_e32 v147, v18, v22, vcc
	v_cndmask_b32_e32 v143, v26, v30, vcc
	v_cndmask_b32_e32 v148, v34, v38, vcc
	v_cndmask_b32_e32 v144, v42, v46, vcc
	v_cndmask_b32_e32 v149, v50, v54, vcc
	v_cndmask_b32_e32 v145, v58, v62, vcc
	v_cmp_ne_u32_e32 vcc, 0, v197
	v_cndmask_b32_e32 v146, v146, v142, vcc
	v_cndmask_b32_e32 v147, v147, v143, vcc
	v_cndmask_b32_e32 v148, v148, v144, vcc
	v_cndmask_b32_e32 v149, v149, v145, vcc
	v_fma_f32 v142, v134, v146, v130
	v_fma_f32 v143, v135, v147, v131
	v_fma_f32 v144, v136, v148, v132
	v_fma_f32 v145, v137, v149, v133
	global_store_dword v[180:181], v142, off
	global_store_dword v[180:181], v143, off offset:256
	global_store_dword v[180:181], v144, off offset:512
	global_store_dword v[180:181], v145, off offset:768
	v_lshl_add_u64 v[180:181], v[180:181], 0, s[48:49]
	s_add_i32 s33, s33, 2
	s_cmp_lt_u32 s33, 8
	s_cbranch_scc1 .Le2_loop
	s_cmp_lt_i32 s35, 0
	s_cbranch_scc1 .Le2_exit
	s_add_i32 s39, s39, s43
	s_add_i32 s39, s39, 7
	v_mov_b32_e32 v180, v182
	v_mov_b32_e32 v181, v183
	v_mov_b32_e32 v134, v138
	v_mov_b32_e32 v135, v139
	v_mov_b32_e32 v136, v140
	v_mov_b32_e32 v137, v141
	s_mov_b32 s33, 0
	s_branch .Le2_loop
